# scan loader: K tile loaded one chunk ahead into spare VGPRs (no wait on fresh loads); conv_store uses permlane32_swap
# baseline (speedup 1.0000x reference)
; __device__ __forceinline__ void p4_scan(const Args& a, const Frame& F) {
;     ...
;             auto conv_load = [&](int it) {
;                 const float* cW; int cN, cn;
;                 if (it < 32768) { const int e = it >> 10, sb = it & 1023; ck0 = (sb >> 6) * 64; cn = (sb & 63) * 32 + (lane & 31); cN = 2048; cW = a.in[IN_W1] + (size_t)e * 1024 * 2048; cD = (bf16*)(a.ws + WS_W1T);
;                     const int up = cn >= 1024, nn = cn & 1023; crow = e * 2048 + (nn >> 7) * 256 + up * 128 + (nn & 127); }
;                 else { const int it2 = it - 32768, e = it2 >> 9, sb = it2 & 511; ck0 = (sb >> 5) * 64; cn = (sb & 31) * 32 + (lane & 31); cN = 1024; cW = a.in[IN_W2] + (size_t)e * 1024 * 1024; cD = (bf16*)(a.ws + WS_W2T); crow = e * 1024 + cn; }
; #pragma unroll
;                 for (int i = 0; i < 32; ++i) cv[i] = cW[(size_t)(ck0 + (lane >> 5) + 2 * i) * cN + cn];
;             };
;     ...
;             conv_load(lw);
.LBB0_490:
	v_and_b32_e32 v82, 0x3c0, v9
	v_or_b32_e32 v14, v82, v158
	v_mov_b32_e32 v9, v145
	v_mul_u32_u24_e32 v12, s54, v14
	v_lshl_add_u64 v[8:9], v[8:9], 2, s[56:57]
	v_lshlrev_b32_e32 v12, 2, v12
	v_mov_b32_e32 v13, v145
	v_lshl_add_u64 v[12:13], v[8:9], 0, v[12:13]
	global_load_dword v148, v[12:13], off
	v_or_b32_e32 v12, 2, v14
	v_mul_u32_u24_e32 v12, s54, v12
	v_lshlrev_b32_e32 v12, 2, v12
	v_mov_b32_e32 v13, v145
	v_lshl_add_u64 v[12:13], v[8:9], 0, v[12:13]
	global_load_dword v141, v[12:13], off
	v_or_b32_e32 v12, 4, v14
	v_mul_u32_u24_e32 v12, s54, v12
	v_lshlrev_b32_e32 v12, 2, v12
	v_mov_b32_e32 v13, v145
	v_lshl_add_u64 v[12:13], v[8:9], 0, v[12:13]
	global_load_dword v149, v[12:13], off
	v_or_b32_e32 v12, 6, v14
	v_mul_u32_u24_e32 v12, s54, v12
	v_lshlrev_b32_e32 v12, 2, v12
	v_mov_b32_e32 v13, v145
	v_lshl_add_u64 v[12:13], v[8:9], 0, v[12:13]
	global_load_dword v137, v[12:13], off
	v_or_b32_e32 v12, 8, v14
	v_mul_u32_u24_e32 v12, s54, v12
	v_lshlrev_b32_e32 v12, 2, v12
	v_mov_b32_e32 v13, v145
	v_lshl_add_u64 v[12:13], v[8:9], 0, v[12:13]
	global_load_dword v142, v[12:13], off
	v_or_b32_e32 v12, 10, v14
	v_mul_u32_u24_e32 v12, s54, v12
	v_lshlrev_b32_e32 v12, 2, v12
	v_mov_b32_e32 v13, v145
	v_lshl_add_u64 v[12:13], v[8:9], 0, v[12:13]
	global_load_dword v81, v[12:13], off
	v_or_b32_e32 v12, 12, v14
	v_mul_u32_u24_e32 v12, s54, v12
	v_lshlrev_b32_e32 v12, 2, v12
	v_mov_b32_e32 v13, v145
	v_lshl_add_u64 v[12:13], v[8:9], 0, v[12:13]
	global_load_dword v138, v[12:13], off
	v_or_b32_e32 v12, 14, v14
	v_mul_u32_u24_e32 v12, s54, v12
	v_lshlrev_b32_e32 v12, 2, v12
	v_mov_b32_e32 v13, v145
	v_lshl_add_u64 v[12:13], v[8:9], 0, v[12:13]
	global_load_dword v151, v[12:13], off
	v_or_b32_e32 v12, 16, v14
	v_mul_u32_u24_e32 v12, s54, v12
	v_lshlrev_b32_e32 v12, 2, v12
	v_mov_b32_e32 v13, v145
	v_lshl_add_u64 v[12:13], v[8:9], 0, v[12:13]
	global_load_dword v152, v[12:13], off
	v_or_b32_e32 v12, 18, v14
	v_mul_u32_u24_e32 v12, s54, v12
	v_lshlrev_b32_e32 v12, 2, v12
	v_mov_b32_e32 v13, v145
	v_lshl_add_u64 v[12:13], v[8:9], 0, v[12:13]
	global_load_dword v143, v[12:13], off
	v_or_b32_e32 v12, 20, v14
	v_mul_u32_u24_e32 v12, s54, v12
	v_lshlrev_b32_e32 v12, 2, v12
	v_mov_b32_e32 v13, v145
	v_lshl_add_u64 v[12:13], v[8:9], 0, v[12:13]
	global_load_dword v150, v[12:13], off
	v_or_b32_e32 v12, 22, v14
	v_mul_u32_u24_e32 v12, s54, v12
	v_lshlrev_b32_e32 v12, 2, v12
	v_mov_b32_e32 v13, v145
	v_lshl_add_u64 v[12:13], v[8:9], 0, v[12:13]
	global_load_dword v139, v[12:13], off
	v_or_b32_e32 v12, 24, v14
	v_mul_u32_u24_e32 v12, s54, v12
	v_lshlrev_b32_e32 v12, 2, v12
	v_mov_b32_e32 v13, v145
	v_lshl_add_u64 v[12:13], v[8:9], 0, v[12:13]
	global_load_dword v147, v[12:13], off
	v_or_b32_e32 v12, 26, v14
	v_mul_u32_u24_e32 v12, s54, v12
	v_lshlrev_b32_e32 v12, 2, v12
	v_mov_b32_e32 v13, v145
	v_lshl_add_u64 v[12:13], v[8:9], 0, v[12:13]
	global_load_dword v83, v[12:13], off
	v_or_b32_e32 v12, 28, v14
	v_mul_u32_u24_e32 v12, s54, v12
	v_lshlrev_b32_e32 v12, 2, v12
	v_mov_b32_e32 v13, v145
	v_lshl_add_u64 v[12:13], v[8:9], 0, v[12:13]
	global_load_dword v140, v[12:13], off
	v_or_b32_e32 v12, 30, v14
	v_mul_u32_u24_e32 v12, s54, v12
	v_lshlrev_b32_e32 v12, 2, v12
	v_mov_b32_e32 v13, v145
	v_lshl_add_u64 v[12:13], v[8:9], 0, v[12:13]
	global_load_dword v153, v[12:13], off
	v_or_b32_e32 v12, 32, v14
	v_mul_u32_u24_e32 v12, s54, v12
	v_lshlrev_b32_e32 v12, 2, v12
	v_mov_b32_e32 v13, v145
	v_lshl_add_u64 v[12:13], v[8:9], 0, v[12:13]
	global_load_dword v183, v[12:13], off
	v_or_b32_e32 v12, 34, v14
	v_mul_u32_u24_e32 v12, s54, v12
	v_lshlrev_b32_e32 v12, 2, v12
	v_mov_b32_e32 v13, v145
	v_lshl_add_u64 v[12:13], v[8:9], 0, v[12:13]
	global_load_dword v179, v[12:13], off
	v_or_b32_e32 v12, 36, v14
	v_mul_u32_u24_e32 v12, s54, v12
	v_lshlrev_b32_e32 v12, 2, v12
	v_mov_b32_e32 v13, v145
	v_lshl_add_u64 v[12:13], v[8:9], 0, v[12:13]
	global_load_dword v184, v[12:13], off
	v_or_b32_e32 v12, 38, v14
	v_mul_u32_u24_e32 v12, s54, v12
	v_lshlrev_b32_e32 v12, 2, v12
	v_mov_b32_e32 v13, v145
	v_lshl_add_u64 v[12:13], v[8:9], 0, v[12:13]
	global_load_dword v175, v[12:13], off
	v_or_b32_e32 v12, 40, v14
	v_mul_u32_u24_e32 v12, s54, v12
	v_lshlrev_b32_e32 v12, 2, v12
	v_mov_b32_e32 v13, v145
	v_lshl_add_u64 v[12:13], v[8:9], 0, v[12:13]
	global_load_dword v180, v[12:13], off
	v_or_b32_e32 v12, 42, v14
	v_mul_u32_u24_e32 v12, s54, v12
	v_lshlrev_b32_e32 v12, 2, v12
	v_mov_b32_e32 v13, v145
	v_lshl_add_u64 v[12:13], v[8:9], 0, v[12:13]
	global_load_dword v173, v[12:13], off
; __device__ __forceinline__ void p4_scan(const Args& a, const Frame& F) {
;     ...
;             auto prefetch = [&](int ci) {
;                 const int base = chunk_base(ci);
; #pragma unroll
;                 for (int i = 0; i < 8; ++i) { const int p = ht + 256 * i, row = p >> 4, c16 = p & 15; const int tok = base + (dir ? 127 - row : row);
;                     pq[i] = *(const u32x4*)(QKC + (size_t)tok * 1024 + h * 128 + c16 * 8); pk[i] = *(const u32x4*)(QKC + (size_t)tok * 1024 + 512 + h * 128 + c16 * 8); }
;     ...
;             auto conv_load = [&](int it) {
;                 const float* cW; int cN, cn;
;                 if (it < 32768) { const int e = it >> 10, sb = it & 1023; ck0 = (sb >> 6) * 64; cn = (sb & 63) * 32 + (lane & 31); cN = 2048; cW = a.in[IN_W1] + (size_t)e * 1024 * 2048; cD = (bf16*)(a.ws + WS_W1T);
;                     const int up = cn >= 1024, nn = cn & 1023; crow = e * 2048 + (nn >> 7) * 256 + up * 128 + (nn & 127); }
;                 else { const int it2 = it - 32768, e = it2 >> 9, sb = it2 & 511; ck0 = (sb >> 5) * 64; cn = (sb & 31) * 32 + (lane & 31); cN = 1024; cW = a.in[IN_W2] + (size_t)e * 1024 * 1024; cD = (bf16*)(a.ws + WS_W2T); crow = e * 1024 + cn; }
; #pragma unroll
;                 for (int i = 0; i < 32; ++i) cv[i] = cW[(size_t)(ck0 + (lane >> 5) + 2 * i) * cN + cn];
;             };
	v_or_b32_e32 v12, 44, v14
	v_mul_u32_u24_e32 v12, s54, v12
	v_lshlrev_b32_e32 v12, 2, v12
	v_mov_b32_e32 v13, v145
	v_lshl_add_u64 v[12:13], v[8:9], 0, v[12:13]
	global_load_dword v176, v[12:13], off
	v_or_b32_e32 v12, 46, v14
	v_mul_u32_u24_e32 v12, s54, v12
	v_lshlrev_b32_e32 v12, 2, v12
	v_mov_b32_e32 v13, v145
	v_lshl_add_u64 v[12:13], v[8:9], 0, v[12:13]
	global_load_dword v186, v[12:13], off
	v_or_b32_e32 v12, 48, v14
	v_mul_u32_u24_e32 v12, s54, v12
	v_lshlrev_b32_e32 v12, 2, v12
	v_mov_b32_e32 v13, v145
	v_lshl_add_u64 v[12:13], v[8:9], 0, v[12:13]
	global_load_dword v187, v[12:13], off
	v_or_b32_e32 v12, 50, v14
	v_mul_u32_u24_e32 v12, s54, v12
	v_lshlrev_b32_e32 v12, 2, v12
	v_mov_b32_e32 v13, v145
	v_lshl_add_u64 v[12:13], v[8:9], 0, v[12:13]
	global_load_dword v181, v[12:13], off
	v_or_b32_e32 v12, 52, v14
	v_mul_u32_u24_e32 v12, s54, v12
	v_lshlrev_b32_e32 v12, 2, v12
	v_mov_b32_e32 v13, v145
	v_lshl_add_u64 v[12:13], v[8:9], 0, v[12:13]
	global_load_dword v185, v[12:13], off
	v_or_b32_e32 v12, 54, v14
	v_mul_u32_u24_e32 v12, s54, v12
	v_lshlrev_b32_e32 v12, 2, v12
	v_mov_b32_e32 v13, v145
	v_lshl_add_u64 v[12:13], v[8:9], 0, v[12:13]
	global_load_dword v177, v[12:13], off
	v_or_b32_e32 v12, 56, v14
	v_mul_u32_u24_e32 v12, s54, v12
	v_lshlrev_b32_e32 v12, 2, v12
	v_mov_b32_e32 v13, v145
	v_lshl_add_u64 v[12:13], v[8:9], 0, v[12:13]
	global_load_dword v182, v[12:13], off
	v_or_b32_e32 v12, 58, v14
	v_mul_u32_u24_e32 v12, s54, v12
	v_lshlrev_b32_e32 v12, 2, v12
	v_mov_b32_e32 v13, v145
	v_lshl_add_u64 v[12:13], v[8:9], 0, v[12:13]
	global_load_dword v174, v[12:13], off
	v_or_b32_e32 v12, 60, v14
	v_mul_u32_u24_e32 v12, s54, v12
	v_lshlrev_b32_e32 v12, 2, v12
	v_mov_b32_e32 v13, v145
	v_lshl_add_u64 v[12:13], v[8:9], 0, v[12:13]
	global_load_dword v178, v[12:13], off
	v_or_b32_e32 v12, 62, v14
	v_mul_u32_u24_e32 v12, s54, v12
	v_lshlrev_b32_e32 v12, 2, v12
	v_mov_b32_e32 v13, v145
	v_lshl_add_u64 v[8:9], v[8:9], 0, v[12:13]
	global_load_dword v188, v[8:9], off
	s_lshl_b32 s44, s44, 1
	s_add_u32 s54, s20, s44
	s_addc_u32 s55, s21, 0
	s_lshl_b32 s33, s33, 1
	s_add_u32 s54, s54, s33
	s_addc_u32 s55, s55, 0
	v_mov_b32_e32 v87, v145
	v_lshl_add_u64 v[86:87], s[54:55], 0, v[86:87]
	s_add_i32 s54, s34, s35
	v_mov_b64_e32 v[8:9], s[38:39]
	s_add_i32 s33, 0, 0x23430
	v_mad_i64_i32 v[88:89], s[34:35], v88, s95, v[8:9]
	v_mad_i64_i32 v[90:91], s[34:35], v90, s95, v[8:9]
	s_add_i32 s54, s54, 0x10000
	v_add_u32_e32 v12, s33, v11
	s_lshl_b32 s33, s58, 13
	s_xor_b32 s34, s54, 0x80
	s_add_u32 s54, s16, s44
	v_add_u32_e32 v11, s89, v11
	s_addc_u32 s55, s17, 0
	v_lshl_add_u64 v[92:93], s[54:55], 0, v[144:145]
	s_mov_b32 s44, 0
	v_mov_b32_e32 v136, 0
	v_add_u32_e32 v134, v12, v10
	v_add_u32_e32 v135, v11, v10
	v_add_u32_e32 v214, s34, v96
	v_ashrrev_i32_e32 v215, 31, v214
	v_lshlrev_b64 v[214:215], 11, v[214:215]
	v_lshl_add_u64 v[214:215], v[92:93], 0, v[214:215]
	global_load_dwordx4 v[220:223], v[214:215], off offset:1024
	v_add_u32_e32 v214, s34, v97
	v_ashrrev_i32_e32 v215, 31, v214
	v_lshlrev_b64 v[214:215], 11, v[214:215]
	v_lshl_add_u64 v[214:215], v[92:93], 0, v[214:215]
	global_load_dwordx4 v[224:227], v[214:215], off offset:1024
	v_add_u32_e32 v214, s34, v98
	v_ashrrev_i32_e32 v215, 31, v214
	v_lshlrev_b64 v[214:215], 11, v[214:215]
	v_lshl_add_u64 v[214:215], v[92:93], 0, v[214:215]
	global_load_dwordx4 v[228:231], v[214:215], off offset:1024
	v_add_u32_e32 v214, s34, v99
	v_ashrrev_i32_e32 v215, 31, v214
	v_lshlrev_b64 v[214:215], 11, v[214:215]
	v_lshl_add_u64 v[214:215], v[92:93], 0, v[214:215]
	global_load_dwordx4 v[232:235], v[214:215], off offset:1024
	v_add_u32_e32 v214, s34, v100
	v_ashrrev_i32_e32 v215, 31, v214
	v_lshlrev_b64 v[214:215], 11, v[214:215]
	v_lshl_add_u64 v[214:215], v[92:93], 0, v[214:215]
	global_load_dwordx4 v[236:239], v[214:215], off offset:1024
	v_add_u32_e32 v214, s34, v101
	v_ashrrev_i32_e32 v215, 31, v214
	v_lshlrev_b64 v[214:215], 11, v[214:215]
	v_lshl_add_u64 v[214:215], v[92:93], 0, v[214:215]
	global_load_dwordx4 v[240:243], v[214:215], off offset:1024
	v_add_u32_e32 v214, s34, v102
	v_ashrrev_i32_e32 v215, 31, v214
	v_lshlrev_b64 v[214:215], 11, v[214:215]
	v_lshl_add_u64 v[214:215], v[92:93], 0, v[214:215]
	global_load_dwordx4 v[244:247], v[214:215], off offset:1024
	v_add_u32_e32 v214, s34, v103
	v_ashrrev_i32_e32 v215, 31, v214
	v_lshlrev_b64 v[214:215], 11, v[214:215]
	v_lshl_add_u64 v[214:215], v[92:93], 0, v[214:215]
	global_load_dwordx4 v[248:251], v[214:215], off offset:1024
	s_branch .LBB0_492

; __device__ __forceinline__ void p4_scan(const Args& a, const Frame& F) {
;     ...
;             auto prefetch = [&](int ci) {
;                 const int base = chunk_base(ci);
; #pragma unroll
;                 for (int i = 0; i < 8; ++i) { const int p = ht + 256 * i, row = p >> 4, c16 = p & 15; const int tok = base + (dir ? 127 - row : row);
;                     pq[i] = *(const u32x4*)(QKC + (size_t)tok * 1024 + h * 128 + c16 * 8); pk[i] = *(const u32x4*)(QKC + (size_t)tok * 1024 + 512 + h * 128 + c16 * 8); }
; #pragma unroll
;                 for (int i = 0; i < 2; ++i) { const int p = ht + 256 * i, row = p >> 2, cc = p & 3; const int tok = base + (dir ? 127 - row : row);
;                     pv[i] = *(const u32x4*)(PV + (size_t)tok * 512 + h * 128 + vs * 32 + cc * 8); pga[i] = GS[(size_t)hd * TA + tok]; }
; #pragma unroll
;                 for (int i = 0; i < 2; ++i) { const int idx = ht + 256 * i; if (idx < 384) { const int row = idx & 127, arr = idx >> 7; const int tok = base + (dir ? 127 - row : row); pgl[i] = GS[(size_t)(arr * 8 + hd) * TA + tok]; } }
;                 pbt = CH[(hd * 528 + (base >> 7)) * 2]; ppx = CH[(hd * 528 + (base >> 7)) * 2 + 1];
;     ...
;             for (int ci = 0; ci < 66; ++ci) {
;                 const float M127 = fmaxf(pmx, mcar), mnew = btot + M127;
;                 const int cnx = ci + 1 < 66 ? ci + 1 : 65;
;                 prefetch(cnx);
.LBB0_492:
	s_waitcnt vmcnt(0)
	s_add_i32 s35, s44, 1
	s_cmpk_eq_i32 s44, 0x41
	s_cselect_b32 s56, s44, s35
	s_sub_i32 s58, 0x41, s56
	v_sub_co_u32_e64 v8, s[54:55], s56, 2
	s_and_b64 s[56:57], s[4:5], exec
	v_readfirstlane_b32 s56, v8
	s_cselect_b32 s56, s56, s58
	s_lshl_b32 s56, s56, 7
	s_add_i32 s56, s56, s33
	s_and_b64 s[54:55], s[54:55], exec
	s_cselect_b32 s56, s34, s56
	v_add_u32_e32 v8, s56, v96
	v_ashrrev_i32_e32 v9, 31, v8
	v_lshlrev_b64 v[8:9], 11, v[8:9]
	v_lshl_add_u64 v[8:9], v[92:93], 0, v[8:9]
	global_load_dwordx4 v[16:19], v[8:9], off
	v_add_u32_e32 v8, s56, v97
	v_ashrrev_i32_e32 v9, 31, v8
	v_lshlrev_b64 v[8:9], 11, v[8:9]
	v_lshl_add_u64 v[8:9], v[92:93], 0, v[8:9]
	global_load_dwordx4 v[20:23], v[8:9], off
	v_add_u32_e32 v8, s56, v98
	v_ashrrev_i32_e32 v9, 31, v8
	v_lshlrev_b64 v[8:9], 11, v[8:9]
	v_lshl_add_u64 v[8:9], v[92:93], 0, v[8:9]
	global_load_dwordx4 v[24:27], v[8:9], off
	v_add_u32_e32 v8, s56, v99
	v_ashrrev_i32_e32 v9, 31, v8
	v_lshlrev_b64 v[8:9], 11, v[8:9]
	v_lshl_add_u64 v[8:9], v[92:93], 0, v[8:9]
	global_load_dwordx4 v[28:31], v[8:9], off
	v_add_u32_e32 v8, s56, v100
	v_ashrrev_i32_e32 v9, 31, v8
	v_lshlrev_b64 v[8:9], 11, v[8:9]
	v_lshl_add_u64 v[8:9], v[92:93], 0, v[8:9]
	global_load_dwordx4 v[32:35], v[8:9], off
	v_add_u32_e32 v8, s56, v101
	v_ashrrev_i32_e32 v9, 31, v8
	v_lshlrev_b64 v[8:9], 11, v[8:9]
	v_lshl_add_u64 v[8:9], v[92:93], 0, v[8:9]
	global_load_dwordx4 v[36:39], v[8:9], off
	v_add_u32_e32 v8, s56, v102
	v_ashrrev_i32_e32 v9, 31, v8
	v_lshlrev_b64 v[8:9], 11, v[8:9]
	v_lshl_add_u64 v[8:9], v[92:93], 0, v[8:9]
	global_load_dwordx4 v[40:43], v[8:9], off
	v_add_u32_e32 v8, s56, v103
	v_ashrrev_i32_e32 v9, 31, v8
	v_lshlrev_b64 v[8:9], 11, v[8:9]
	v_lshl_add_u64 v[8:9], v[92:93], 0, v[8:9]
	global_load_dwordx4 v[44:47], v[8:9], off
	v_add_u32_e32 v8, s56, v104
	v_ashrrev_i32_e32 v9, 31, v8
	v_lshlrev_b64 v[10:11], 10, v[8:9]
	v_lshl_add_u64 v[10:11], v[86:87], 0, v[10:11]
	v_lshl_add_u64 v[8:9], v[8:9], 2, s[50:51]
	global_load_dwordx4 v[12:15], v[10:11], off
	global_load_dword v172, v[8:9], off
	v_add_u32_e32 v8, s56, v105
	v_ashrrev_i32_e32 v9, 31, v8
	v_lshlrev_b64 v[10:11], 10, v[8:9]
	v_lshl_add_u64 v[10:11], v[86:87], 0, v[10:11]
	v_lshl_add_u64 v[94:95], v[8:9], 2, s[50:51]
	global_load_dwordx4 v[8:11], v[10:11], off
	s_nop 0
	global_load_dword v171, v[94:95], off
	v_or_b32_e32 v94, s56, v106
	v_ashrrev_i32_e32 v95, 31, v94
	s_and_saveexec_b64 s[54:55], s[6:7]
	s_cbranch_execz .LBB0_494
	v_lshl_add_u64 v[190:191], v[94:95], 2, v[88:89]
	global_load_dword v108, v[190:191], off

; #define LAS __attribute__((address_space(3)))
; __device__ __forceinline__ float bflo(unsigned w) { return __uint_as_float(w << 16); }
; __device__ __forceinline__ void p4_scan(const Args& a, const Frame& F) {
;     ...
;                 pbt = CH[(hd * 528 + (base >> 7)) * 2]; ppx = CH[(hd * 528 + (base >> 7)) * 2 + 1];
;             };
;             auto commitK = [&](int kbuf) {
; #pragma unroll
;                 for (int i = 0; i < 8; ++i) { const int p = ht + 256 * i, row = p >> 4, c16 = p & 15; *(LAS u32x4*)(L + kbuf + row * SP + c16 * 16) = pk[i]; } };
;             auto commitQ = [&]() {
; #pragma unroll
;                 for (int i = 0; i < 8; ++i) { const int p = ht + 256 * i, row = p >> 4, c16 = p & 15; *(LAS u32x4*)(L + S_QS + row * SP + c16 * 16) = pq[i]; } };
;             auto commitV = [&](float mprev, int vabuf) {
; #pragma unroll
;                 for (int i = 0; i < 2; ++i) { const int p = ht + 256 * i, row = p >> 2, cc = p & 3; const unsigned wv[4] = {pv[i].x, pv[i].y, pv[i].z, pv[i].w};
;                     const float av = __expf(pga[i] - fmaxf(ppx, mprev));
; #pragma unroll
;                     for (int j = 0; j < 4; ++j) { const unsigned sc2 = pg8::cvt_pk_bf16(av * bflo(wv[j]), av * bfhi(wv[j]));
;                         *(LAS bf16*)(L + S_VT + (cc * 8 + 2 * j) * SP + row * 2) = (bf16)(wv[j] & 0xffffu); *(LAS bf16*)(L + S_VT + (cc * 8 + 2 * j + 1) * SP + row * 2) = (bf16)(wv[j] >> 16);
;                         *(LAS bf16*)(L + vabuf + (cc * 8 + 2 * j) * SP + row * 2) = (bf16)(sc2 & 0xffffu); *(LAS bf16*)(L + vabuf + (cc * 8 + 2 * j + 1) * SP + row * 2) = (bf16)(sc2 >> 16); }
;                     if (cc == 0) *(LAS bf16*)(L + vabuf + 32 * SP + row * 2) = (bf16)f2bf(av); }
; #pragma unroll
;                 for (int i = 0; i < 2; ++i) { const int idx = ht + 256 * i; if (idx < 384) { const int row = idx & 127, arr = idx >> 7; *(LAS float*)(L + S_GL + arr * 512 + row * 4) = pgl[i]; } }
;             };
;             prefetch(0);
;             LDS_BARRIER();
;             commitK(S_K0); commitQ(); commitV(0.f, S_VA0);
;             float btot = pbt, pmx = ppx;
;             LDS_BARRIER();
;             const int lw = blk * 4 + (w - 4);
;             float cv[32]; bf16* cD = nullptr; int ck0 = 0, crow = 0;
;             auto conv_load = [&](int it) {
;                 const float* cW; int cN, cn;
.LBB0_496:
	s_or_b64 exec, exec, s[54:55]
	s_ashr_i32 s54, s56, 7
	s_add_i32 s54, s54, s76
	s_lshl_b32 s54, s54, 1
	s_ashr_i32 s55, s54, 31
	s_lshl_b64 s[54:55], s[54:55], 2
	s_add_u32 s54, s60, s54
	s_addc_u32 s55, s61, s55
	global_load_dwordx2 v[94:95], v145, s[54:55]
	s_bitcmp0_b32 s44, 0
	s_cselect_b64 s[54:55], -1, 0
	s_and_b64 s[56:57], s[54:55], exec
	s_cselect_b32 s56, 0x11000, s91
	s_add_i32 s56, s56, 0
	v_add3_u32 v144, s56, v109, v117
	ds_write_b128 v144, v[220:223]
	v_add3_u32 v48, s56, v110, v117
	ds_write_b128 v48, v[224:227]
	v_add3_u32 v48, s56, v111, v117
	ds_write_b128 v48, v[228:231]
	v_add3_u32 v48, s56, v112, v117
	ds_write_b128 v48, v[232:235]
	v_add3_u32 v48, s56, v113, v117
	ds_write_b128 v48, v[236:239]
	v_add3_u32 v48, s56, v114, v117
	ds_write_b128 v48, v[240:243]
	v_add3_u32 v48, s56, v115, v117
	ds_write_b128 v48, v[244:247]
	v_add3_u32 v48, s56, v116, v117
	s_cmp_gt_u32 s44, 47
	ds_write_b128 v48, v[248:251]
	s_cbranch_scc1 .LBB0_498
	v_permlane32_swap_b32_e32 v148, v183
	v_cvt_pk_bf16_f32 v48, v148, v183
	v_permlane32_swap_b32_e32 v141, v179
	v_cvt_pk_bf16_f32 v49, v141, v179
	v_permlane32_swap_b32_e32 v149, v184
	v_cvt_pk_bf16_f32 v50, v149, v184
	v_permlane32_swap_b32_e32 v137, v175
	v_cvt_pk_bf16_f32 v51, v137, v175
	v_permlane32_swap_b32_e32 v142, v180
	v_cvt_pk_bf16_f32 v52, v142, v180
	v_permlane32_swap_b32_e32 v81, v173
	v_cvt_pk_bf16_f32 v53, v81, v173
	v_permlane32_swap_b32_e32 v138, v176
	v_ashrrev_i32_e32 v81, 31, v80
	v_cvt_pk_bf16_f32 v54, v138, v176
	v_permlane32_swap_b32_e32 v151, v186
	v_cvt_pk_bf16_f32 v55, v151, v186
	v_permlane32_swap_b32_e32 v152, v187
	v_cvt_pk_bf16_f32 v56, v152, v187
	v_permlane32_swap_b32_e32 v143, v181
	v_cvt_pk_bf16_f32 v57, v143, v181
	v_permlane32_swap_b32_e32 v150, v185
	v_cvt_pk_bf16_f32 v58, v150, v185
	v_permlane32_swap_b32_e32 v139, v177
	v_cvt_pk_bf16_f32 v59, v139, v177
	v_permlane32_swap_b32_e32 v147, v182
	v_cvt_pk_bf16_f32 v60, v147, v182
	v_permlane32_swap_b32_e32 v83, v174
	v_mov_b32_e32 v147, v145
	v_cvt_pk_bf16_f32 v61, v83, v174
	v_permlane32_swap_b32_e32 v140, v178
	v_mov_b32_e32 v83, v145
	v_cvt_pk_bf16_f32 v62, v140, v178
	v_permlane32_swap_b32_e32 v153, v188
	v_cvt_pk_bf16_f32 v63, v153, v188
	v_lshlrev_b64 v[64:65], 11, v[80:81]
	v_lshl_add_u64 v[64:65], s[52:53], 0, v[64:65]
	v_lshl_add_u64 v[64:65], v[82:83], 1, v[64:65]
	v_lshl_add_u64 v[64:65], v[64:65], 0, v[146:147]
	global_store_dwordx4 v[64:65], v[48:51], off
	global_store_dwordx4 v[64:65], v[52:55], off offset:16
	global_store_dwordx4 v[64:65], v[56:59], off offset:32
	global_store_dwordx4 v[64:65], v[60:63], off offset:48
.LBB0_498:
	s_add_i32 s98, s35, 1
	s_min_i32 s98, s98, 0x41
	s_sub_i32 s99, 0x41, s98
	s_add_i32 s98, s98, -2
	s_and_b64 s[100:101], s[4:5], exec
	s_cselect_b32 s98, s98, s99
	s_lshl_b32 s98, s98, 7
	s_add_i32 s98, s98, s33
	v_add_u32_e32 v214, s98, v96
	v_ashrrev_i32_e32 v215, 31, v214
	v_lshlrev_b64 v[214:215], 11, v[214:215]
	v_lshl_add_u64 v[214:215], v[92:93], 0, v[214:215]
	global_load_dwordx4 v[220:223], v[214:215], off offset:1024
	v_add_u32_e32 v214, s98, v97
	v_ashrrev_i32_e32 v215, 31, v214
	v_lshlrev_b64 v[214:215], 11, v[214:215]
	v_lshl_add_u64 v[214:215], v[92:93], 0, v[214:215]
	global_load_dwordx4 v[224:227], v[214:215], off offset:1024
	v_add_u32_e32 v214, s98, v98
	v_ashrrev_i32_e32 v215, 31, v214
	v_lshlrev_b64 v[214:215], 11, v[214:215]
	v_lshl_add_u64 v[214:215], v[92:93], 0, v[214:215]
	global_load_dwordx4 v[228:231], v[214:215], off offset:1024
	v_add_u32_e32 v214, s98, v99
	v_ashrrev_i32_e32 v215, 31, v214
	v_lshlrev_b64 v[214:215], 11, v[214:215]
	v_lshl_add_u64 v[214:215], v[92:93], 0, v[214:215]
	global_load_dwordx4 v[232:235], v[214:215], off offset:1024
	v_add_u32_e32 v214, s98, v100
	v_ashrrev_i32_e32 v215, 31, v214
	v_lshlrev_b64 v[214:215], 11, v[214:215]
	v_lshl_add_u64 v[214:215], v[92:93], 0, v[214:215]
	global_load_dwordx4 v[236:239], v[214:215], off offset:1024
	v_add_u32_e32 v214, s98, v101
	v_ashrrev_i32_e32 v215, 31, v214
	v_lshlrev_b64 v[214:215], 11, v[214:215]
	v_lshl_add_u64 v[214:215], v[92:93], 0, v[214:215]
	global_load_dwordx4 v[240:243], v[214:215], off offset:1024
	v_add_u32_e32 v214, s98, v102
	v_ashrrev_i32_e32 v215, 31, v214
	v_lshlrev_b64 v[214:215], 11, v[214:215]
	v_lshl_add_u64 v[214:215], v[92:93], 0, v[214:215]
	global_load_dwordx4 v[244:247], v[214:215], off offset:1024
	v_add_u32_e32 v214, s98, v103
	v_ashrrev_i32_e32 v215, 31, v214
	v_lshlrev_b64 v[214:215], 11, v[214:215]
	v_lshl_add_u64 v[214:215], v[92:93], 0, v[214:215]
	global_load_dwordx4 v[248:251], v[214:215], off offset:1024
	s_sub_i32 s52, s35, 48
	s_cmp_lt_u32 s44, 47
	s_cselect_b32 s44, s35, s52
	s_lshl_b32 s64, s44, 10
	s_add_i32 s64, s64, s77
	s_cmpk_gt_i32 s64, 0x7fff
	s_mov_b64 s[52:53], -1
	s_cbranch_scc0 .LBB0_500
	s_add_i32 s44, s64, 0xffff8000
	s_lshr_b32 s44, s44, 9
	s_lshl_b32 s56, s64, 1
	s_lshl_b64 s[52:53], s[44:45], 22
	s_add_u32 s58, s28, s52
	s_addc_u32 s59, s29, s53
	v_lshl_add_u32 v80, s44, 10, v133
	s_mov_b64 s[52:53], 0
	v_mov_b32_e32 v48, s56

; #define LDS_BARRIER() do { asm volatile("s_waitcnt lgkmcnt(0)" ::: "memory"); __builtin_amdgcn_s_barrier(); asm volatile("" ::: "memory"); } while (0)
; __device__ __forceinline__ void p4_scan(const Args& a, const Frame& F) {
;     ...
;             auto conv_load = [&](int it) {
;                 const float* cW; int cN, cn;
;                 if (it < 32768) { const int e = it >> 10, sb = it & 1023; ck0 = (sb >> 6) * 64; cn = (sb & 63) * 32 + (lane & 31); cN = 2048; cW = a.in[IN_W1] + (size_t)e * 1024 * 2048; cD = (bf16*)(a.ws + WS_W1T);
;                     const int up = cn >= 1024, nn = cn & 1023; crow = e * 2048 + (nn >> 7) * 256 + up * 128 + (nn & 127); }
;                 else { const int it2 = it - 32768, e = it2 >> 9, sb = it2 & 511; ck0 = (sb >> 5) * 64; cn = (sb & 31) * 32 + (lane & 31); cN = 1024; cW = a.in[IN_W2] + (size_t)e * 1024 * 1024; cD = (bf16*)(a.ws + WS_W2T); crow = e * 1024 + cn; }
; #pragma unroll
;                 for (int i = 0; i < 32; ++i) cv[i] = cW[(size_t)(ck0 + (lane >> 5) + 2 * i) * cN + cn];
;             };
;     ...
;                 const float M127 = fmaxf(pmx, mcar), mnew = btot + M127;
;                 const int cnx = ci + 1 < 66 ? ci + 1 : 65;
;                 prefetch(cnx);
;                 commitK((ci & 1) ? S_K0 : S_K1);
;                 if (ci < 48) conv_store();
;                 conv_load(lw + 1024 * ((ci + 1) % 48));
;                 LDS_BARRIER();
.LBB0_502:
	v_and_b32_e32 v82, 0x3c0, v48
	v_max_f32_e32 v49, v136, v136
	v_max_f32_e32 v50, v85, v85
	v_or_b32_e32 v52, v82, v158
	v_max_f32_e32 v49, v50, v49
	v_mul_u32_u24_e32 v50, s56, v52
	v_add_f32_e32 v136, v84, v49
	v_lshl_add_u64 v[48:49], v[144:145], 2, s[58:59]
	v_lshlrev_b32_e32 v144, 2, v50
	v_lshl_add_u64 v[50:51], v[48:49], 0, v[144:145]
	global_load_dword v148, v[50:51], off
	v_or_b32_e32 v50, 2, v52
	v_mul_u32_u24_e32 v50, s56, v50
	v_lshlrev_b32_e32 v144, 2, v50
	v_lshl_add_u64 v[50:51], v[48:49], 0, v[144:145]
	global_load_dword v141, v[50:51], off
	v_or_b32_e32 v50, 4, v52
	v_mul_u32_u24_e32 v50, s56, v50
	v_lshlrev_b32_e32 v144, 2, v50
	v_lshl_add_u64 v[50:51], v[48:49], 0, v[144:145]
	global_load_dword v149, v[50:51], off
	v_or_b32_e32 v50, 6, v52
	v_mul_u32_u24_e32 v50, s56, v50
	v_lshlrev_b32_e32 v144, 2, v50
	v_lshl_add_u64 v[50:51], v[48:49], 0, v[144:145]
	global_load_dword v137, v[50:51], off
	v_or_b32_e32 v50, 8, v52
	v_mul_u32_u24_e32 v50, s56, v50
	v_lshlrev_b32_e32 v144, 2, v50
	v_lshl_add_u64 v[50:51], v[48:49], 0, v[144:145]
	global_load_dword v142, v[50:51], off
	v_or_b32_e32 v50, 10, v52
	v_mul_u32_u24_e32 v50, s56, v50
	v_lshlrev_b32_e32 v144, 2, v50
	v_lshl_add_u64 v[50:51], v[48:49], 0, v[144:145]
	global_load_dword v81, v[50:51], off
	v_or_b32_e32 v50, 12, v52
	v_mul_u32_u24_e32 v50, s56, v50
	v_lshlrev_b32_e32 v144, 2, v50
	v_lshl_add_u64 v[50:51], v[48:49], 0, v[144:145]
	global_load_dword v138, v[50:51], off
	v_or_b32_e32 v50, 14, v52
	v_mul_u32_u24_e32 v50, s56, v50
	v_lshlrev_b32_e32 v144, 2, v50
	v_lshl_add_u64 v[50:51], v[48:49], 0, v[144:145]
	global_load_dword v151, v[50:51], off
	v_or_b32_e32 v50, 16, v52
	v_mul_u32_u24_e32 v50, s56, v50
	v_lshlrev_b32_e32 v144, 2, v50
	v_lshl_add_u64 v[50:51], v[48:49], 0, v[144:145]
	global_load_dword v152, v[50:51], off
	v_or_b32_e32 v50, 18, v52
	v_mul_u32_u24_e32 v50, s56, v50
	v_lshlrev_b32_e32 v144, 2, v50
	v_lshl_add_u64 v[50:51], v[48:49], 0, v[144:145]
	global_load_dword v143, v[50:51], off
	v_or_b32_e32 v50, 20, v52
	v_mul_u32_u24_e32 v50, s56, v50
	v_lshlrev_b32_e32 v144, 2, v50
	v_lshl_add_u64 v[50:51], v[48:49], 0, v[144:145]
	global_load_dword v150, v[50:51], off
	v_or_b32_e32 v50, 22, v52
	v_mul_u32_u24_e32 v50, s56, v50
	v_lshlrev_b32_e32 v144, 2, v50
	v_lshl_add_u64 v[50:51], v[48:49], 0, v[144:145]
	global_load_dword v139, v[50:51], off
	v_or_b32_e32 v50, 24, v52
	v_mul_u32_u24_e32 v50, s56, v50
	v_lshlrev_b32_e32 v144, 2, v50
	v_lshl_add_u64 v[50:51], v[48:49], 0, v[144:145]
	global_load_dword v147, v[50:51], off
	v_or_b32_e32 v50, 26, v52
	v_mul_u32_u24_e32 v50, s56, v50
	v_lshlrev_b32_e32 v144, 2, v50
	v_lshl_add_u64 v[50:51], v[48:49], 0, v[144:145]
	global_load_dword v83, v[50:51], off
	v_or_b32_e32 v50, 28, v52
	v_mul_u32_u24_e32 v50, s56, v50
	v_lshlrev_b32_e32 v144, 2, v50
	v_lshl_add_u64 v[50:51], v[48:49], 0, v[144:145]
	global_load_dword v140, v[50:51], off
	v_or_b32_e32 v50, 30, v52
	v_mul_u32_u24_e32 v50, s56, v50
	v_lshlrev_b32_e32 v144, 2, v50
	v_lshl_add_u64 v[50:51], v[48:49], 0, v[144:145]
	global_load_dword v153, v[50:51], off
	v_or_b32_e32 v50, 32, v52
	v_mul_u32_u24_e32 v50, s56, v50
	v_lshlrev_b32_e32 v144, 2, v50
	v_lshl_add_u64 v[50:51], v[48:49], 0, v[144:145]
	global_load_dword v183, v[50:51], off
	v_or_b32_e32 v50, 34, v52
	v_mul_u32_u24_e32 v50, s56, v50
	v_lshlrev_b32_e32 v144, 2, v50
	v_lshl_add_u64 v[50:51], v[48:49], 0, v[144:145]
	global_load_dword v179, v[50:51], off
	v_or_b32_e32 v50, 36, v52
	v_mul_u32_u24_e32 v50, s56, v50
	v_lshlrev_b32_e32 v144, 2, v50
	v_lshl_add_u64 v[50:51], v[48:49], 0, v[144:145]
	global_load_dword v184, v[50:51], off
	v_or_b32_e32 v50, 38, v52
	v_mul_u32_u24_e32 v50, s56, v50
	v_lshlrev_b32_e32 v144, 2, v50
	v_lshl_add_u64 v[50:51], v[48:49], 0, v[144:145]
	global_load_dword v175, v[50:51], off
	v_or_b32_e32 v50, 40, v52
	v_mul_u32_u24_e32 v50, s56, v50
	v_lshlrev_b32_e32 v144, 2, v50
	v_lshl_add_u64 v[50:51], v[48:49], 0, v[144:145]
	global_load_dword v180, v[50:51], off
	v_or_b32_e32 v50, 42, v52
	v_mul_u32_u24_e32 v50, s56, v50
	v_lshlrev_b32_e32 v144, 2, v50
	v_lshl_add_u64 v[50:51], v[48:49], 0, v[144:145]
	global_load_dword v173, v[50:51], off
	v_or_b32_e32 v50, 44, v52
	v_mul_u32_u24_e32 v50, s56, v50
	v_lshlrev_b32_e32 v144, 2, v50
	v_lshl_add_u64 v[50:51], v[48:49], 0, v[144:145]
	global_load_dword v176, v[50:51], off
	v_or_b32_e32 v50, 46, v52
	v_mul_u32_u24_e32 v50, s56, v50
	v_lshlrev_b32_e32 v144, 2, v50
	v_lshl_add_u64 v[50:51], v[48:49], 0, v[144:145]
	global_load_dword v186, v[50:51], off
	v_or_b32_e32 v50, 48, v52
	v_mul_u32_u24_e32 v50, s56, v50
	v_lshlrev_b32_e32 v144, 2, v50
	v_lshl_add_u64 v[50:51], v[48:49], 0, v[144:145]
	global_load_dword v187, v[50:51], off
	v_or_b32_e32 v50, 50, v52
	v_mul_u32_u24_e32 v50, s56, v50
	v_lshlrev_b32_e32 v144, 2, v50
	v_lshl_add_u64 v[50:51], v[48:49], 0, v[144:145]
	global_load_dword v181, v[50:51], off
	v_or_b32_e32 v50, 52, v52
	v_mul_u32_u24_e32 v50, s56, v50
	v_lshlrev_b32_e32 v144, 2, v50
	v_lshl_add_u64 v[50:51], v[48:49], 0, v[144:145]
	global_load_dword v185, v[50:51], off
	v_or_b32_e32 v50, 54, v52
	v_mul_u32_u24_e32 v50, s56, v50
	v_lshlrev_b32_e32 v144, 2, v50
	v_lshl_add_u64 v[50:51], v[48:49], 0, v[144:145]
	global_load_dword v177, v[50:51], off
	v_or_b32_e32 v50, 56, v52
	v_mul_u32_u24_e32 v50, s56, v50
	v_lshlrev_b32_e32 v144, 2, v50
	v_lshl_add_u64 v[50:51], v[48:49], 0, v[144:145]
	global_load_dword v182, v[50:51], off
	v_or_b32_e32 v50, 58, v52
	v_mul_u32_u24_e32 v50, s56, v50
	v_lshlrev_b32_e32 v144, 2, v50
	v_lshl_add_u64 v[50:51], v[48:49], 0, v[144:145]
	global_load_dword v174, v[50:51], off
	v_or_b32_e32 v50, 60, v52
	v_mul_u32_u24_e32 v50, s56, v50
	v_lshlrev_b32_e32 v144, 2, v50
	v_lshl_add_u64 v[50:51], v[48:49], 0, v[144:145]
	global_load_dword v178, v[50:51], off
	v_or_b32_e32 v50, 62, v52
	v_mul_u32_u24_e32 v50, s56, v50
	v_lshlrev_b32_e32 v144, 2, v50
	v_lshl_add_u64 v[48:49], v[48:49], 0, v[144:145]
	global_load_dword v188, v[48:49], off
	s_waitcnt lgkmcnt(0)
	s_barrier
; #define LAS __attribute__((address_space(3)))
; __device__ __forceinline__ unsigned f2bf(float f) { unsigned u = __builtin_bit_cast(unsigned, f); return (u + 0x7fffu + ((u >> 16) & 1u)) >> 16; }
; __device__ __forceinline__ float bflo(unsigned w) { return __uint_as_float(w << 16); }
; __device__ __forceinline__ float bfhi(unsigned w) { return __uint_as_float(w & 0xffff0000u); }
; __device__ __forceinline__ unsigned cvt_pk_bf16(float lo, float hi) { unsigned r; asm volatile("v_cvt_pk_bf16_f32 %0, %1, %2" : "=v"(r) : "v"(lo), "v"(hi)); return r; }
; __device__ __forceinline__ void p4_scan(const Args& a, const Frame& F) {
;     ...
;             auto commitQ = [&]() {
; #pragma unroll
;                 for (int i = 0; i < 8; ++i) { const int p = ht + 256 * i, row = p >> 4, c16 = p & 15; *(LAS u32x4*)(L + S_QS + row * SP + c16 * 16) = pq[i]; } };
;             auto commitV = [&](float mprev, int vabuf) {
; #pragma unroll
;                 for (int i = 0; i < 2; ++i) { const int p = ht + 256 * i, row = p >> 2, cc = p & 3; const unsigned wv[4] = {pv[i].x, pv[i].y, pv[i].z, pv[i].w};
;                     const float av = __expf(pga[i] - fmaxf(ppx, mprev));
; #pragma unroll
;                     for (int j = 0; j < 4; ++j) { const unsigned sc2 = pg8::cvt_pk_bf16(av * bflo(wv[j]), av * bfhi(wv[j]));
;                         *(LAS bf16*)(L + S_VT + (cc * 8 + 2 * j) * SP + row * 2) = (bf16)(wv[j] & 0xffffu); *(LAS bf16*)(L + S_VT + (cc * 8 + 2 * j + 1) * SP + row * 2) = (bf16)(wv[j] >> 16);
;                         *(LAS bf16*)(L + vabuf + (cc * 8 + 2 * j) * SP + row * 2) = (bf16)(sc2 & 0xffffu); *(LAS bf16*)(L + vabuf + (cc * 8 + 2 * j + 1) * SP + row * 2) = (bf16)(sc2 >> 16); }
;                     if (cc == 0) *(LAS bf16*)(L + vabuf + 32 * SP + row * 2) = (bf16)f2bf(av); }
; #pragma unroll
;                 for (int i = 0; i < 2; ++i) { const int idx = ht + 256 * i; if (idx < 384) { const int row = idx & 127, arr = idx >> 7; *(LAS float*)(L + S_GL + arr * 512 + row * 4) = pgl[i]; } }
;             };
;     ...
;                 mcar = mnew;
;                 commitQ(); commitV(mcar, (ci & 1) ? S_VA0 : S_VA1); btot = pbt; pmx = ppx;
	s_waitcnt vmcnt(40)
	ds_write_b128 v119, v[16:19]
	ds_write_b128 v120, v[20:23]
	ds_write_b128 v121, v[24:27]
	ds_write_b128 v122, v[28:31]
	ds_write_b128 v123, v[32:35]
	ds_write_b128 v124, v[36:39]
	ds_write_b128 v125, v[40:43]
	ds_write_b128 v126, v[44:47]
	v_max_f32_e32 v16, v95, v95
	v_max_f32_e32 v16, v16, v136
	v_sub_f32_e32 v17, v172, v16
	v_mul_f32_e32 v17, 0x3fb8aa3b, v17
	v_exp_f32_e32 v17, v17
	s_and_b64 s[54:55], s[54:55], exec
	v_lshlrev_b32_e32 v18, 16, v12
	v_and_b32_e32 v19, 0xffff0000, v12
	s_cselect_b32 s44, 0x1de20, s92
	v_mul_f32_e32 v18, v17, v18
	v_mul_f32_e32 v19, v17, v19
	v_cvt_pk_bf16_f32 v18, v18, v19
	v_add_u32_e32 v19, v128, v129
	s_add_i32 s44, s44, 0
	ds_write_b16 v127, v12
	ds_write_b16_d16_hi v19, v12 offset:272
	v_add_u32_e32 v12, s44, v129
	v_add_u32_e32 v20, v12, v118
	ds_write_b16 v20, v18
	ds_write_b16_d16_hi v20, v18 offset:272
	v_lshlrev_b32_e32 v18, 16, v13
	v_mul_f32_e32 v18, v17, v18
	v_and_b32_e32 v21, 0xffff0000, v13
	v_mul_f32_e32 v21, v17, v21
	v_cvt_pk_bf16_f32 v18, v18, v21
	ds_write_b16 v19, v13 offset:544
	ds_write_b16_d16_hi v19, v13 offset:816
	ds_write_b16 v20, v18 offset:544
	ds_write_b16_d16_hi v20, v18 offset:816
	v_lshlrev_b32_e32 v13, 16, v14
	v_mul_f32_e32 v13, v17, v13
	v_and_b32_e32 v18, 0xffff0000, v14
	v_mul_f32_e32 v18, v17, v18
	v_cvt_pk_bf16_f32 v13, v13, v18
	ds_write_b16 v19, v14 offset:1088
	ds_write_b16_d16_hi v19, v14 offset:1360
	ds_write_b16 v20, v13 offset:1088
	ds_write_b16_d16_hi v20, v13 offset:1360
	v_lshlrev_b32_e32 v13, 16, v15
	v_mul_f32_e32 v13, v17, v13
	v_and_b32_e32 v14, 0xffff0000, v15
	v_mul_f32_e32 v14, v17, v14
	v_cvt_pk_bf16_f32 v13, v13, v14
	ds_write_b16 v19, v15 offset:1632
	ds_write_b16_d16_hi v19, v15 offset:1904
	ds_write_b16 v20, v13 offset:1632
	ds_write_b16_d16_hi v20, v13 offset:1904
	s_and_saveexec_b64 s[54:55], s[10:11]
	v_bfe_u32 v13, v17, 16, 1
	v_add3_u32 v13, v17, v13, s93
	v_add_u32_e32 v14, s44, v118
	ds_write_b16_d16_hi v14, v13 offset:8704
	s_or_b64 exec, exec, s[54:55]
	v_sub_f32_e32 v13, v171, v16
	v_mul_f32_e32 v13, 0x3fb8aa3b, v13
	v_exp_f32_e32 v13, v13
	v_lshlrev_b32_e32 v14, 16, v8
	v_and_b32_e32 v15, 0xffff0000, v8
	v_mul_f32_e32 v14, v13, v14
	v_mul_f32_e32 v15, v13, v15
	v_cvt_pk_bf16_f32 v14, v14, v15
	ds_write_b16 v131, v8
	ds_write_b16_d16_hi v132, v8 offset:272
	v_add_u32_e32 v8, v12, v130
	v_lshlrev_b32_e32 v12, 16, v9
	ds_write_b16 v8, v14
	ds_write_b16_d16_hi v8, v14 offset:272
	v_mul_f32_e32 v12, v13, v12
	v_and_b32_e32 v14, 0xffff0000, v9
	v_mul_f32_e32 v14, v13, v14
	v_cvt_pk_bf16_f32 v12, v12, v14
	ds_write_b16 v132, v9 offset:544
	ds_write_b16_d16_hi v132, v9 offset:816
	ds_write_b16 v8, v12 offset:544
	ds_write_b16_d16_hi v8, v12 offset:816
	v_lshlrev_b32_e32 v9, 16, v10
	v_mul_f32_e32 v9, v13, v9
	v_and_b32_e32 v12, 0xffff0000, v10
	v_mul_f32_e32 v12, v13, v12
	v_cvt_pk_bf16_f32 v9, v9, v12
	ds_write_b16 v132, v10 offset:1088
	ds_write_b16_d16_hi v132, v10 offset:1360
	ds_write_b16 v8, v9 offset:1088
	ds_write_b16_d16_hi v8, v9 offset:1360
	v_lshlrev_b32_e32 v9, 16, v11
	v_mul_f32_e32 v9, v13, v9
	v_and_b32_e32 v10, 0xffff0000, v11
	v_mul_f32_e32 v10, v13, v10
	v_cvt_pk_bf16_f32 v9, v9, v10
	ds_write_b16 v132, v11 offset:1632
	ds_write_b16_d16_hi v132, v11 offset:1904
	ds_write_b16 v8, v9 offset:1632
	ds_write_b16_d16_hi v8, v9 offset:1904
	s_and_saveexec_b64 s[54:55], s[10:11]
	s_cbranch_execnz .LBB0_507
	s_or_b64 exec, exec, s[54:55]
	s_and_saveexec_b64 s[54:55], s[6:7]
	s_cbranch_execnz .LBB0_508

; #define LAS __attribute__((address_space(3)))
; __global__ void __launch_bounds__(512, 2) mk_fwd(Args args) {
;     extern __shared__ __attribute__((aligned(16))) unsigned char lds_raw[];
;     Frame F;
;     F.lds = (LAS unsigned char*)lds_raw; F.misc = F.lds + LDS_MAIN;
;     F.tid = threadIdx.x; F.lane = F.tid & 63; F.wave = __builtin_amdgcn_readfirstlane(F.tid >> 6); F.G = gridDim.x; F.bid = blockIdx.x;
	.amdhsa_kernel _Z6mk_fwd4Args
		.amdhsa_group_segment_fixed_size 0
		.amdhsa_private_segment_fixed_size 0
		.amdhsa_kernarg_size 480
		.amdhsa_user_sgpr_count 2
		.amdhsa_user_sgpr_dispatch_ptr 0
		.amdhsa_user_sgpr_queue_ptr 0
		.amdhsa_user_sgpr_kernarg_segment_ptr 1
		.amdhsa_user_sgpr_dispatch_id 0
		.amdhsa_user_sgpr_kernarg_preload_length 0
		.amdhsa_user_sgpr_kernarg_preload_offset 0
		.amdhsa_user_sgpr_private_segment_size 0
		.amdhsa_uses_dynamic_stack 0
		.amdhsa_enable_private_segment 0
		.amdhsa_system_sgpr_workgroup_id_x 1
		.amdhsa_system_sgpr_workgroup_id_y 0
		.amdhsa_system_sgpr_workgroup_id_z 0
		.amdhsa_system_sgpr_workgroup_info 0
		.amdhsa_system_vgpr_workitem_id 0
		.amdhsa_next_free_vgpr 256
		.amdhsa_next_free_sgpr 102
		.amdhsa_accum_offset 256
		.amdhsa_reserve_vcc 1
		.amdhsa_float_round_mode_32 0
		.amdhsa_float_round_mode_16_64 0
		.amdhsa_float_denorm_mode_32 3
		.amdhsa_float_denorm_mode_16_64 3
		.amdhsa_dx10_clamp 1
		.amdhsa_ieee_mode 1
		.amdhsa_fp16_overflow 0
		.amdhsa_tg_split 0
		.amdhsa_exception_fp_ieee_invalid_op 0
		.amdhsa_exception_fp_denorm_src 0
		.amdhsa_exception_fp_ieee_div_zero 0
		.amdhsa_exception_fp_ieee_overflow 0
		.amdhsa_exception_fp_ieee_underflow 0
		.amdhsa_exception_fp_ieee_inexact 0
		.amdhsa_exception_int_div_zero 0
	.end_amdhsa_kernel

; #define LAS __attribute__((address_space(3)))
; __global__ void __launch_bounds__(512, 2) mk_fwd(Args args) {
;     extern __shared__ __attribute__((aligned(16))) unsigned char lds_raw[];
;     Frame F;
;     F.lds = (LAS unsigned char*)lds_raw; F.misc = F.lds + LDS_MAIN;
;     F.tid = threadIdx.x; F.lane = F.tid & 63; F.wave = __builtin_amdgcn_readfirstlane(F.tid >> 6); F.G = gridDim.x; F.bid = blockIdx.x;
amdhsa.kernels:
  - .agpr_count:     0
    .args:
      - .offset:         0
        .size:           224
        .value_kind:     by_value
      - .offset:         224
        .size:           4
        .value_kind:     hidden_block_count_x
      - .offset:         228
        .size:           4
        .value_kind:     hidden_block_count_y
      - .offset:         232
        .size:           4
        .value_kind:     hidden_block_count_z
      - .offset:         236
        .size:           2
        .value_kind:     hidden_group_size_x
      - .offset:         238
        .size:           2
        .value_kind:     hidden_group_size_y
      - .offset:         240
        .size:           2
        .value_kind:     hidden_group_size_z
      - .offset:         242
        .size:           2
        .value_kind:     hidden_remainder_x
      - .offset:         244
        .size:           2
        .value_kind:     hidden_remainder_y
      - .offset:         246
        .size:           2
        .value_kind:     hidden_remainder_z
      - .offset:         264
        .size:           8
        .value_kind:     hidden_global_offset_x
      - .offset:         272
        .size:           8
        .value_kind:     hidden_global_offset_y
      - .offset:         280
        .size:           8
        .value_kind:     hidden_global_offset_z
      - .offset:         288
        .size:           2
        .value_kind:     hidden_grid_dims
      - .offset:         344
        .size:           4
        .value_kind:     hidden_dynamic_lds_size
    .group_segment_fixed_size: 0
    .kernarg_segment_align: 8
    .kernarg_segment_size: 480
    .language:       OpenCL C
    .language_version:
      - 2
      - 0
    .max_flat_workgroup_size: 512
    .name:           _Z6mk_fwd4Args
    .private_segment_fixed_size: 0
    .sgpr_count:     108
    .sgpr_spill_count: 11
    .symbol:         _Z6mk_fwd4Args.kd
    .uniform_work_group_size: 1
    .uses_dynamic_stack: false
    .vgpr_count:     256
    .vgpr_spill_count: 0
    .wavefront_size: 64
